# grid barrier: non-last XCD leaders poll TOP >= (tg+1)*nx directly instead of the last leader's TOPGEN bump (one memory hop less); on top of m16
# baseline (speedup 1.0000x reference)
; DI unsigned xb_ld(unsigned* p)              { return __hip_atomic_load(p, __ATOMIC_RELAXED, __HIP_MEMORY_SCOPE_AGENT); }
; DI unsigned xb_add(unsigned* p, unsigned v) { return __hip_atomic_fetch_add(p, v, __ATOMIC_RELAXED, __HIP_MEMORY_SCOPE_AGENT); }
; #define XB_SPIN(cond, bar) do { unsigned _sp = 0; while (cond) { __builtin_amdgcn_s_sleep(1); \
;     if ((++_sp & 255u) == 0u) { if (xb_ld(&(bar)[XB_TMO])) break; if (_sp > XB_SPIN_CAP) { atomicAdd(&(bar)[XB_TMO], 1u); break; } } } } while (0)
; DI void xcd_barrier(const XcdBarrier& b) {
;     ...
;         const unsigned old = xb_add(&bar[XB_XSUB(b.x)], 1u);
;         const unsigned gen = old / nloc;
;         if (old + 1u == (gen + 1u) * nloc) {
;             __builtin_amdgcn_fence(__ATOMIC_RELEASE, "agent");
;             asm volatile("s_waitcnt vmcnt(0)" ::: "memory");
;             const unsigned og = xb_add(&bar[XB_TOP], 1u);
;             const unsigned tg = og / nx;
;             if (og + 1u == (tg + 1u) * nx) xb_add(&bar[XB_TOPGEN], 1u);
;             else XB_SPIN(xb_ld(&bar[XB_TOPGEN]) == tg, bar);
.LBB0_243:
	s_andn2_saveexec_b64 s[4:5], s[30:31]
	s_cbranch_execz .LBB0_259
	v_readlane_b32 s4, v254, 14
	v_readlane_b32 s5, v254, 15
	buffer_wbl2 sc1
	s_waitcnt vmcnt(0)
	v_mov_b32_e32 v1, 1
	v_mov_b64_e32 v[6:7], s[4:5]
	flat_atomic_add v1, v[6:7], v1 sc0
	v_cvt_f32_u32_e32 v3, v2
	v_sub_u32_e32 v5, 0, v2
	s_mov_b64 s[40:41], -1
	v_rcp_iflag_f32_e32 v3, v3
	s_nop 0
	v_mul_f32_e32 v3, 0x4f7ffffe, v3
	v_cvt_u32_f32_e32 v3, v3
	v_mul_lo_u32 v5, v5, v3
	v_mul_hi_u32 v5, v3, v5
	v_add_u32_e32 v3, v3, v5
	s_waitcnt vmcnt(0) lgkmcnt(0)
	v_mul_hi_u32 v3, v1, v3
	v_mul_lo_u32 v6, v3, v2
	v_add_u32_e32 v5, 1, v1
	v_sub_u32_e32 v1, v1, v6
	v_add_u32_e32 v7, 1, v3
	v_cmp_ge_u32_e32 vcc, v1, v2
	v_sub_u32_e32 v6, v1, v2
	s_nop 0
	v_cndmask_b32_e32 v3, v3, v7, vcc
	v_cndmask_b32_e32 v1, v1, v6, vcc
	v_add_u32_e32 v6, 1, v3
	v_cmp_ge_u32_e32 vcc, v1, v2
	s_nop 1
	v_cndmask_b32_e32 v1, v3, v6, vcc
	v_mad_u64_u32 v[2:3], s[4:5], v2, v1, v[2:3]
	v_mov_b32_e32 v21, v2
	v_readlane_b32 s4, v254, 16
	v_readlane_b32 s5, v254, 17
	v_cmp_ne_u32_e32 vcc, v5, v2
	s_nop 0
	v_mov_b64_e32 v[2:3], s[4:5]
	s_and_saveexec_b64 s[30:31], vcc
	s_cbranch_execz .LBB0_256
	v_readlane_b32 s4, v254, 14
	v_readlane_b32 s5, v254, 15
	s_mov_b64 s[42:43], 0
	s_nop 0
	v_mov_b64_e32 v[2:3], s[4:5]
	flat_load_dword v2, v[2:3] sc1
	s_waitcnt vmcnt(0) lgkmcnt(0)
	v_cmp_lt_u32_e32 vcc, v2, v21
	s_and_saveexec_b64 s[40:41], vcc
	s_cbranch_execz .LBB0_255
	s_mov_b32 s1, 1
	s_branch .LBB0_248

; DI unsigned xb_ld(unsigned* p)              { return __hip_atomic_load(p, __ATOMIC_RELAXED, __HIP_MEMORY_SCOPE_AGENT); }
; #define XB_SPIN(cond, bar) do { unsigned _sp = 0; while (cond) { __builtin_amdgcn_s_sleep(1); \
;     if ((++_sp & 255u) == 0u) { if (xb_ld(&(bar)[XB_TMO])) break; if (_sp > XB_SPIN_CAP) { atomicAdd(&(bar)[XB_TMO], 1u); break; } } } } while (0)
; DI void xcd_barrier(const XcdBarrier& b) {
;     ...
;             else XB_SPIN(xb_ld(&bar[XB_TOPGEN]) == tg, bar);
.LBB0_253:
	v_readlane_b32 s4, v254, 14
	v_readlane_b32 s5, v254, 15
	s_add_i32 s1, s1, 1
	s_or_b64 s[48:49], s[48:49], exec
	v_mov_b64_e32 v[2:3], s[4:5]
	flat_load_dword v2, v[2:3] sc1
	s_waitcnt vmcnt(0) lgkmcnt(0)
	v_cmp_ge_u32_e32 vcc, v2, v21
	s_orn2_b64 s[46:47], vcc, exec
	s_branch .LBB0_247

; DI unsigned xb_ld(unsigned* p)              { return __hip_atomic_load(p, __ATOMIC_RELAXED, __HIP_MEMORY_SCOPE_AGENT); }
; DI unsigned xb_add(unsigned* p, unsigned v) { return __hip_atomic_fetch_add(p, v, __ATOMIC_RELAXED, __HIP_MEMORY_SCOPE_AGENT); }
; #define XB_SPIN(cond, bar) do { unsigned _sp = 0; while (cond) { __builtin_amdgcn_s_sleep(1); \
;     if ((++_sp & 255u) == 0u) { if (xb_ld(&(bar)[XB_TMO])) break; if (_sp > XB_SPIN_CAP) { atomicAdd(&(bar)[XB_TMO], 1u); break; } } } } while (0)
; DI void xcd_barrier(const XcdBarrier& b) {
;     ...
;         const unsigned old = xb_add(&bar[XB_XSUB(b.x)], 1u);
;         const unsigned gen = old / nloc;
;         if (old + 1u == (gen + 1u) * nloc) {
;             __builtin_amdgcn_fence(__ATOMIC_RELEASE, "agent");
;             asm volatile("s_waitcnt vmcnt(0)" ::: "memory");
;             const unsigned og = xb_add(&bar[XB_TOP], 1u);
;             const unsigned tg = og / nx;
;             if (og + 1u == (tg + 1u) * nx) xb_add(&bar[XB_TOPGEN], 1u);
;             else XB_SPIN(xb_ld(&bar[XB_TOPGEN]) == tg, bar);
.LBB0_543:
	s_andn2_saveexec_b64 s[6:7], s[30:31]
	s_cbranch_execz .LBB0_559
	v_readlane_b32 s6, v254, 14
	v_readlane_b32 s7, v254, 15
	buffer_wbl2 sc1
	s_waitcnt vmcnt(0)
	v_mov_b32_e32 v1, 1
	v_mov_b64_e32 v[6:7], s[6:7]
	flat_atomic_add v3, v[6:7], v1 sc0
	v_cvt_f32_u32_e32 v1, v2
	v_sub_u32_e32 v5, 0, v2
	s_mov_b64 s[40:41], -1
	v_rcp_iflag_f32_e32 v1, v1
	s_nop 0
	v_mul_f32_e32 v1, 0x4f7ffffe, v1
	v_cvt_u32_f32_e32 v1, v1
	v_mul_lo_u32 v5, v5, v1
	v_mul_hi_u32 v5, v1, v5
	v_add_u32_e32 v1, v1, v5
	s_waitcnt vmcnt(0) lgkmcnt(0)
	v_mul_hi_u32 v1, v3, v1
	v_mul_lo_u32 v5, v1, v2
	v_sub_u32_e32 v5, v3, v5
	v_cmp_ge_u32_e32 vcc, v5, v2
	v_add_u32_e32 v6, 1, v1
	s_nop 0
	v_cndmask_b32_e32 v1, v1, v6, vcc
	v_sub_u32_e32 v6, v5, v2
	v_cndmask_b32_e32 v5, v5, v6, vcc
	v_cmp_ge_u32_e32 vcc, v5, v2
	v_add_u32_e32 v5, 1, v1
	s_nop 0
	v_cndmask_b32_e32 v1, v1, v5, vcc
	v_add_u32_e32 v5, 1, v3
	v_mad_u64_u32 v[2:3], s[6:7], v2, v1, v[2:3]
	v_mov_b32_e32 v21, v2
	v_readlane_b32 s6, v254, 16
	v_readlane_b32 s7, v254, 17
	v_cmp_ne_u32_e32 vcc, v5, v2
	s_nop 0
	v_mov_b64_e32 v[2:3], s[6:7]
	s_and_saveexec_b64 s[30:31], vcc
	s_cbranch_execz .LBB0_556
	v_readlane_b32 s6, v254, 14
	v_readlane_b32 s7, v254, 15
	s_mov_b64 s[42:43], 0
	s_nop 0
	v_mov_b64_e32 v[2:3], s[6:7]
	flat_load_dword v2, v[2:3] sc1
	s_waitcnt vmcnt(0) lgkmcnt(0)
	v_cmp_lt_u32_e32 vcc, v2, v21
	s_and_saveexec_b64 s[40:41], vcc
	s_cbranch_execz .LBB0_555
	s_mov_b32 s5, 1
	s_branch .LBB0_548

; DI unsigned xb_ld(unsigned* p)              { return __hip_atomic_load(p, __ATOMIC_RELAXED, __HIP_MEMORY_SCOPE_AGENT); }
; #define XB_SPIN(cond, bar) do { unsigned _sp = 0; while (cond) { __builtin_amdgcn_s_sleep(1); \
;     if ((++_sp & 255u) == 0u) { if (xb_ld(&(bar)[XB_TMO])) break; if (_sp > XB_SPIN_CAP) { atomicAdd(&(bar)[XB_TMO], 1u); break; } } } } while (0)
; DI void xcd_barrier(const XcdBarrier& b) {
;     ...
;             else XB_SPIN(xb_ld(&bar[XB_TOPGEN]) == tg, bar);
.LBB0_553:
	v_readlane_b32 s6, v254, 14
	v_readlane_b32 s7, v254, 15
	s_add_i32 s5, s5, 1
	s_or_b64 s[48:49], s[48:49], exec
	v_mov_b64_e32 v[2:3], s[6:7]
	flat_load_dword v2, v[2:3] sc1
	s_waitcnt vmcnt(0) lgkmcnt(0)
	v_cmp_ge_u32_e32 vcc, v2, v21
	s_orn2_b64 s[46:47], vcc, exec
	s_branch .LBB0_547

; DI unsigned xb_ld(unsigned* p)              { return __hip_atomic_load(p, __ATOMIC_RELAXED, __HIP_MEMORY_SCOPE_AGENT); }
; DI unsigned xb_add(unsigned* p, unsigned v) { return __hip_atomic_fetch_add(p, v, __ATOMIC_RELAXED, __HIP_MEMORY_SCOPE_AGENT); }
; #define XB_SPIN(cond, bar) do { unsigned _sp = 0; while (cond) { __builtin_amdgcn_s_sleep(1); \
;     if ((++_sp & 255u) == 0u) { if (xb_ld(&(bar)[XB_TMO])) break; if (_sp > XB_SPIN_CAP) { atomicAdd(&(bar)[XB_TMO], 1u); break; } } } } while (0)
; DI void xcd_barrier(const XcdBarrier& b) {
;     ...
;         const unsigned old = xb_add(&bar[XB_XSUB(b.x)], 1u);
;         const unsigned gen = old / nloc;
;         if (old + 1u == (gen + 1u) * nloc) {
;             __builtin_amdgcn_fence(__ATOMIC_RELEASE, "agent");
;             asm volatile("s_waitcnt vmcnt(0)" ::: "memory");
;             const unsigned og = xb_add(&bar[XB_TOP], 1u);
;             const unsigned tg = og / nx;
;             if (og + 1u == (tg + 1u) * nx) xb_add(&bar[XB_TOPGEN], 1u);
;             else XB_SPIN(xb_ld(&bar[XB_TOPGEN]) == tg, bar);
.LBB0_1084:
	v_readlane_b32 s4, v254, 14
	v_readlane_b32 s5, v254, 15
	buffer_wbl2 sc1
	s_waitcnt vmcnt(0)
	v_mov_b32_e32 v1, 1
	v_mov_b64_e32 v[6:7], s[4:5]
	flat_atomic_add v3, v[6:7], v1 sc0
	v_cvt_f32_u32_e32 v1, v2
	v_sub_u32_e32 v5, 0, v2
	s_mov_b64 s[30:31], -1
	v_rcp_iflag_f32_e32 v1, v1
	s_nop 0
	v_mul_f32_e32 v1, 0x4f7ffffe, v1
	v_cvt_u32_f32_e32 v1, v1
	v_mul_lo_u32 v5, v5, v1
	v_mul_hi_u32 v5, v1, v5
	v_add_u32_e32 v1, v1, v5
	s_waitcnt vmcnt(0) lgkmcnt(0)
	v_mul_hi_u32 v1, v3, v1
	v_mul_lo_u32 v5, v1, v2
	v_sub_u32_e32 v5, v3, v5
	v_cmp_ge_u32_e32 vcc, v5, v2
	v_add_u32_e32 v6, 1, v1
	s_nop 0
	v_cndmask_b32_e32 v1, v1, v6, vcc
	v_sub_u32_e32 v6, v5, v2
	v_cndmask_b32_e32 v5, v5, v6, vcc
	v_cmp_ge_u32_e32 vcc, v5, v2
	v_add_u32_e32 v5, 1, v1
	s_nop 0
	v_cndmask_b32_e32 v1, v1, v5, vcc
	v_add_u32_e32 v5, 1, v3
	v_mad_u64_u32 v[2:3], s[4:5], v2, v1, v[2:3]
	v_mov_b32_e32 v21, v2
	v_readlane_b32 s4, v254, 16
	v_readlane_b32 s5, v254, 17
	v_cmp_ne_u32_e32 vcc, v5, v2
	s_nop 0
	v_mov_b64_e32 v[2:3], s[4:5]
	s_and_saveexec_b64 s[16:17], vcc
	s_cbranch_execz .LBB0_1096
	v_readlane_b32 s4, v254, 14
	v_readlane_b32 s5, v254, 15
	s_mov_b64 s[40:41], 0
	s_nop 0
	v_mov_b64_e32 v[2:3], s[4:5]
	flat_load_dword v2, v[2:3] sc1
	s_waitcnt vmcnt(0) lgkmcnt(0)
	v_cmp_lt_u32_e32 vcc, v2, v21
	s_and_saveexec_b64 s[30:31], vcc
	s_cbranch_execz .LBB0_1095
	s_mov_b32 s4, 1
	s_branch .LBB0_1088

; DI unsigned xb_ld(unsigned* p)              { return __hip_atomic_load(p, __ATOMIC_RELAXED, __HIP_MEMORY_SCOPE_AGENT); }
; #define XB_SPIN(cond, bar) do { unsigned _sp = 0; while (cond) { __builtin_amdgcn_s_sleep(1); \
;     if ((++_sp & 255u) == 0u) { if (xb_ld(&(bar)[XB_TMO])) break; if (_sp > XB_SPIN_CAP) { atomicAdd(&(bar)[XB_TMO], 1u); break; } } } } while (0)
; DI void xcd_barrier(const XcdBarrier& b) {
;     ...
;             else XB_SPIN(xb_ld(&bar[XB_TOPGEN]) == tg, bar);
.LBB0_1093:
	v_readlane_b32 s6, v254, 14
	v_readlane_b32 s7, v254, 15
	s_add_i32 s4, s4, 1
	s_or_b64 s[46:47], s[46:47], exec
	v_mov_b64_e32 v[2:3], s[6:7]
	flat_load_dword v2, v[2:3] sc1
	s_waitcnt vmcnt(0) lgkmcnt(0)
	v_cmp_ge_u32_e32 vcc, v2, v21
	s_orn2_b64 s[44:45], vcc, exec
	s_branch .LBB0_1087
